# baseline (speedup 1.0000x reference)
_Z9ln_kernelILi2EEvPKiPKfS3_PfS3_S3_PDF16_:
	s_load_dwordx4 s[12:15], s[0:1], 0x20
	v_and_b32_e32 v62, 63, v0
	v_lshlrev_b32_e32 v62, 4, v62
	s_load_dwordx8 s[4:11], s[0:1], 0x8
	v_and_b32_e32 v12, 63, v0
	v_lshrrev_b32_e32 v0, 6, v0
	v_lshl_or_b32 v6, s2, 2, v0
	v_ashrrev_i32_e32 v7, 31, v6
	v_lshlrev_b64 v[2:3], 11, v[6:7]
	v_mov_b32_e32 v1, 0
	s_waitcnt lgkmcnt(0)
	global_load_dwordx4 v[64:67], v62, s[12:13]
	global_load_dwordx4 v[68:71], v62, s[12:13] offset:1024
	global_load_dwordx4 v[72:75], v62, s[12:13] offset:2048
	global_load_dwordx4 v[76:79], v62, s[12:13] offset:3072
	global_load_dwordx4 v[80:83], v62, s[14:15]
	global_load_dwordx4 v[84:87], v62, s[14:15] offset:1024
	global_load_dwordx4 v[88:91], v62, s[14:15] offset:2048
	global_load_dwordx4 v[92:95], v62, s[14:15] offset:3072
	v_lshl_add_u64 v[8:9], s[4:5], 0, v[2:3]
	v_lshlrev_b32_e32 v4, 3, v12
	v_mov_b32_e32 v5, v1
	v_lshl_add_u64 v[8:9], v[8:9], 0, v[4:5]
	s_mov_b64 s[2:3], 0x400000
	v_lshl_add_u64 v[10:11], v[8:9], 0, s[2:3]
	s_mov_b32 s2, 0x400000
	global_load_dwordx2 v[16:17], v[8:9], off
	global_load_dwordx2 v[18:19], v[8:9], off offset:512
	global_load_dwordx2 v[20:21], v[8:9], off offset:1024
	global_load_dwordx2 v[22:23], v[8:9], off offset:1536
	v_add_co_u32_e32 v8, vcc, s2, v8
	global_load_dwordx2 v[24:25], v[10:11], off offset:512
	global_load_dwordx2 v[26:27], v[10:11], off offset:1024
	global_load_dwordx2 v[28:29], v[10:11], off offset:1536
	v_addc_co_u32_e32 v9, vcc, 0, v9, vcc
	global_load_dwordx2 v[30:31], v[8:9], off
	v_lshlrev_b64 v[6:7], 12, v[6:7]
	v_lshlrev_b32_e32 v0, 4, v12
	v_lshl_add_u64 v[6:7], s[8:9], 0, v[6:7]
	v_lshl_add_u64 v[6:7], v[6:7], 0, v[0:1]
	global_load_dwordx4 v[8:11], v[6:7], off offset:1024
	global_load_dwordx4 v[12:15], v0, s[6:7] offset:1024
	s_waitcnt vmcnt(9)
	v_cvt_f32_f16_e32 v32, v16
	s_waitcnt vmcnt(8)
	v_cvt_f32_f16_e32 v36, v18
	v_cvt_f32_f16_sdwa v37, v18 dst_sel:DWORD dst_unused:UNUSED_PAD src0_sel:WORD_1
	v_cvt_f32_f16_e32 v38, v19
	v_cvt_f32_f16_sdwa v39, v19 dst_sel:DWORD dst_unused:UNUSED_PAD src0_sel:WORD_1
	s_waitcnt vmcnt(7)
	v_cvt_f32_f16_e32 v40, v20
	v_cvt_f32_f16_sdwa v41, v20 dst_sel:DWORD dst_unused:UNUSED_PAD src0_sel:WORD_1
	v_cvt_f32_f16_e32 v42, v21
	v_cvt_f32_f16_sdwa v43, v21 dst_sel:DWORD dst_unused:UNUSED_PAD src0_sel:WORD_1
	s_waitcnt vmcnt(6)
	v_cvt_f32_f16_e32 v44, v22
	v_cvt_f32_f16_sdwa v45, v22 dst_sel:DWORD dst_unused:UNUSED_PAD src0_sel:WORD_1
	v_cvt_f32_f16_e32 v46, v23
	v_cvt_f32_f16_sdwa v47, v23 dst_sel:DWORD dst_unused:UNUSED_PAD src0_sel:WORD_1
	s_waitcnt vmcnt(5)
	v_cvt_f32_f16_e32 v20, v24
	v_cvt_f32_f16_sdwa v21, v24 dst_sel:DWORD dst_unused:UNUSED_PAD src0_sel:WORD_1
	v_cvt_f32_f16_e32 v22, v25
	v_cvt_f32_f16_sdwa v23, v25 dst_sel:DWORD dst_unused:UNUSED_PAD src0_sel:WORD_1
	s_waitcnt vmcnt(4)
	v_cvt_f32_f16_e32 v24, v26
	v_cvt_f32_f16_sdwa v25, v26 dst_sel:DWORD dst_unused:UNUSED_PAD src0_sel:WORD_1
	v_cvt_f32_f16_e32 v26, v27
	v_cvt_f32_f16_sdwa v27, v27 dst_sel:DWORD dst_unused:UNUSED_PAD src0_sel:WORD_1
	s_waitcnt vmcnt(3)
	v_cvt_f32_f16_e32 v48, v28
	v_cvt_f32_f16_sdwa v49, v28 dst_sel:DWORD dst_unused:UNUSED_PAD src0_sel:WORD_1
	v_cvt_f32_f16_e32 v28, v29
	v_cvt_f32_f16_sdwa v29, v29 dst_sel:DWORD dst_unused:UNUSED_PAD src0_sel:WORD_1
	v_cvt_f32_f16_sdwa v33, v16 dst_sel:DWORD dst_unused:UNUSED_PAD src0_sel:WORD_1
	v_cvt_f32_f16_e32 v34, v17
	v_cvt_f32_f16_sdwa v35, v17 dst_sel:DWORD dst_unused:UNUSED_PAD src0_sel:WORD_1
	s_waitcnt vmcnt(2)
	v_cvt_f32_f16_e32 v50, v30
	v_cvt_f32_f16_sdwa v51, v30 dst_sel:DWORD dst_unused:UNUSED_PAD src0_sel:WORD_1
	v_cvt_f32_f16_e32 v52, v31
	v_cvt_f32_f16_sdwa v53, v31 dst_sel:DWORD dst_unused:UNUSED_PAD src0_sel:WORD_1
	global_load_dwordx4 v[16:19], v[6:7], off
	v_pk_add_f32 v[36:37], v[36:37], v[20:21]
	v_pk_add_f32 v[38:39], v[38:39], v[22:23]
	global_load_dwordx4 v[20:23], v[6:7], off offset:2048
	v_pk_add_f32 v[40:41], v[40:41], v[24:25]
	v_pk_add_f32 v[42:43], v[42:43], v[26:27]
	global_load_dwordx4 v[24:27], v[6:7], off offset:3072
	v_pk_add_f32 v[46:47], v[46:47], v[28:29]
	global_load_dwordx4 v[28:31], v0, s[6:7] offset:2048
	s_waitcnt vmcnt(5)
	v_pk_add_f32 v[36:37], v[8:9], v[36:37]
	v_pk_add_f32 v[38:39], v[10:11], v[38:39]
	global_load_dwordx4 v[8:11], v0, s[6:7]
	v_pk_add_f32 v[44:45], v[44:45], v[48:49]
	v_pk_add_f32 v[48:49], v[32:33], v[50:51]
	v_pk_add_f32 v[50:51], v[34:35], v[52:53]
	global_load_dwordx4 v[32:35], v0, s[6:7] offset:3072
	s_waitcnt vmcnt(6)
	v_pk_add_f32 v[12:13], v[12:13], v[36:37]
	v_pk_add_f32 v[14:15], v[14:15], v[38:39]
	s_load_dwordx4 s[4:7], s[0:1], 0x28
	s_mov_b32 s0, 0xf800000
	s_waitcnt lgkmcnt(0)
	v_lshl_add_u64 v[2:3], s[6:7], 0, v[2:3]
	s_waitcnt vmcnt(4)
	v_pk_add_f32 v[20:21], v[20:21], v[40:41]
	v_pk_add_f32 v[22:23], v[22:23], v[42:43]
	v_pk_add_f32 v[40:41], v[16:17], v[48:49]
	v_pk_add_f32 v[42:43], v[18:19], v[50:51]
	s_waitcnt vmcnt(3)
	v_pk_add_f32 v[24:25], v[24:25], v[44:45]
	v_pk_add_f32 v[26:27], v[26:27], v[46:47]
	s_waitcnt vmcnt(2)
	v_pk_add_f32 v[16:17], v[28:29], v[20:21]
	v_pk_add_f32 v[18:19], v[30:31], v[22:23]
	s_waitcnt vmcnt(1)
	v_pk_add_f32 v[8:9], v[8:9], v[40:41]
	v_pk_add_f32 v[10:11], v[10:11], v[42:43]
	v_mov_b32_e32 v28, v13
	v_mov_b32_e32 v29, v15
	s_waitcnt vmcnt(0)
	v_pk_add_f32 v[20:21], v[32:33], v[24:25]
	v_pk_add_f32 v[22:23], v[34:35], v[26:27]
	v_mov_b32_e32 v24, v8
	v_mov_b32_e32 v25, v10
	v_mov_b32_e32 v26, v9
	v_mov_b32_e32 v27, v11
	v_pk_add_f32 v[24:25], v[24:25], v[26:27]
	v_mov_b32_e32 v26, v12
	v_mov_b32_e32 v27, v14
	v_pk_add_f32 v[26:27], v[26:27], v[28:29]
	v_add_f32_e32 v1, v24, v25
	v_pk_add_f32 v[26:27], v[26:27], v[26:27] op_sel:[0,1] op_sel_hi:[1,0]
	v_pk_add_f32 v[28:29], v[16:17], v[16:17] op_sel:[0,1] op_sel_hi:[1,0]
	v_pk_add_f32 v[30:31], v[18:19], v[18:19] op_sel:[0,1] op_sel_hi:[1,0]
	v_add_f32_e32 v24, 0, v1
	v_mov_b32_e32 v25, v20
	v_mov_b32_e32 v27, v21
	v_mov_b32_e32 v29, v22
	v_mov_b32_e32 v31, v23
	v_pk_add_f32 v[24:25], v[24:25], v[26:27]
	v_pk_add_f32 v[26:27], v[28:29], v[30:31]
	s_nop 0
	v_pk_add_f32 v[24:25], v[24:25], v[26:27]
	s_nop 0
	v_add_f32_e32 v1, v24, v25
	v_mbcnt_lo_u32_b32 v24, -1, 0
	v_mbcnt_hi_u32_b32 v24, -1, v24
	v_and_b32_e32 v25, 64, v24
	v_add_u32_e32 v25, 64, v25
	v_xor_b32_e32 v26, 32, v24
	v_cmp_lt_i32_e32 vcc, v26, v25
	s_nop 1
	v_cndmask_b32_e32 v26, v24, v26, vcc
	v_lshlrev_b32_e32 v52, 2, v26
	ds_bpermute_b32 v26, v52, v1
	s_waitcnt lgkmcnt(0)
	v_add_f32_e32 v1, v1, v26
	v_xor_b32_e32 v26, 16, v24
	v_cmp_lt_i32_e32 vcc, v26, v25
	s_nop 1
	v_cndmask_b32_e32 v26, v24, v26, vcc
	v_lshlrev_b32_e32 v53, 2, v26
	ds_bpermute_b32 v26, v53, v1
	s_waitcnt lgkmcnt(0)
	v_add_f32_e32 v1, v1, v26
	v_xor_b32_e32 v26, 8, v24
	v_cmp_lt_i32_e32 vcc, v26, v25
	s_nop 1
	v_cndmask_b32_e32 v26, v24, v26, vcc
	v_lshlrev_b32_e32 v54, 2, v26
	s_waitcnt lgkmcnt(0)
	s_nop 1
	v_add_f32_dpp v1, v1, v1 row_ror:8 row_mask:0xf bank_mask:0xf
	v_xor_b32_e32 v26, 4, v24
	v_cmp_lt_i32_e32 vcc, v26, v25
	s_nop 1
	v_cndmask_b32_e32 v26, v24, v26, vcc
	v_lshlrev_b32_e32 v55, 2, v26
	s_waitcnt lgkmcnt(0)
	s_nop 1
	v_add_f32_dpp v1, v1, v1 row_ror:4 row_mask:0xf bank_mask:0xf
	v_xor_b32_e32 v26, 2, v24
	v_cmp_lt_i32_e32 vcc, v26, v25
	s_nop 1
	v_cndmask_b32_e32 v26, v24, v26, vcc
	v_lshlrev_b32_e32 v56, 2, v26
	s_waitcnt lgkmcnt(0)
	s_nop 1
	v_add_f32_dpp v1, v1, v1 row_ror:2 row_mask:0xf bank_mask:0xf
	v_xor_b32_e32 v26, 1, v24
	v_cmp_lt_i32_e32 vcc, v26, v25
	s_nop 1
	v_cndmask_b32_e32 v24, v24, v26, vcc
	v_lshlrev_b32_e32 v57, 2, v24
	s_waitcnt lgkmcnt(0)
	s_nop 1
	v_add_f32_dpp v1, v1, v1 row_ror:1 row_mask:0xf bank_mask:0xf
	v_mul_f32_e32 v24, 0x3a800000, v1
	v_pk_add_f32 v[36:37], v[8:9], v[24:25] op_sel_hi:[1,0] neg_lo:[0,1] neg_hi:[0,1]
	v_pk_add_f32 v[38:39], v[10:11], v[24:25] op_sel_hi:[1,0] neg_lo:[0,1] neg_hi:[0,1]
	v_mov_b32_e32 v28, v37
	v_mov_b32_e32 v29, v39
	v_pk_add_f32 v[40:41], v[12:13], v[24:25] op_sel_hi:[1,0] neg_lo:[0,1] neg_hi:[0,1]
	v_pk_add_f32 v[42:43], v[14:15], v[24:25] op_sel_hi:[1,0] neg_lo:[0,1] neg_hi:[0,1]
	v_mov_b32_e32 v26, v36
	v_mov_b32_e32 v27, v38
	v_pk_mul_f32 v[28:29], v[28:29], v[28:29]
	v_mov_b32_e32 v30, v41
	v_mov_b32_e32 v31, v43
	v_pk_fma_f32 v[26:27], v[26:27], v[26:27], v[28:29]
	v_mov_b32_e32 v28, v40
	v_mov_b32_e32 v29, v42
	v_pk_mul_f32 v[30:31], v[30:31], v[30:31]
	v_pk_add_f32 v[44:45], v[16:17], v[24:25] op_sel_hi:[1,0] neg_lo:[0,1] neg_hi:[0,1]
	v_pk_fma_f32 v[28:29], v[28:29], v[28:29], v[30:31]
	v_mul_f32_e32 v30, v44, v44
	v_pk_fma_f32 v[30:31], v[44:45], v[44:45], v[30:31] op_sel_hi:[1,1,0]
	v_pk_add_f32 v[46:47], v[18:19], v[24:25] op_sel_hi:[1,0] neg_lo:[0,1] neg_hi:[0,1]
	v_pk_add_f32 v[48:49], v[20:21], v[24:25] op_sel_hi:[1,0] neg_lo:[0,1] neg_hi:[0,1]
	v_mul_f32_e32 v30, v46, v46
	v_pk_add_f32 v[50:51], v[22:23], v[24:25] op_sel_hi:[1,0] neg_lo:[0,1] neg_hi:[0,1]
	v_pk_fma_f32 v[32:33], v[46:47], v[46:47], v[30:31] op_sel_hi:[1,1,0]
	v_pk_mul_f32 v[34:35], v[48:49], v[48:49]
	v_pk_add_f32 v[26:27], v[26:27], v[26:27] op_sel_hi:[0,1]
	v_pk_add_f32 v[28:29], v[28:29], v[28:29] op_sel_hi:[0,1]
	v_pk_mul_f32 v[24:25], v[50:51], v[50:51]
	v_mov_b32_e32 v30, v34
	v_mov_b32_e32 v32, v35
	v_mov_b32_e32 v26, v24
	v_mov_b32_e32 v28, v25
	v_pk_add_f32 v[30:31], v[30:31], v[32:33]
	v_pk_add_f32 v[24:25], v[26:27], v[28:29]
	s_nop 0
	v_pk_add_f32 v[24:25], v[30:31], v[24:25]
	s_nop 0
	v_add_f32_e32 v1, v24, v25
	ds_bpermute_b32 v24, v52, v1
	s_waitcnt lgkmcnt(0)
	v_add_f32_e32 v1, v1, v24
	ds_bpermute_b32 v24, v53, v1
	s_waitcnt lgkmcnt(0)
	v_add_f32_e32 v1, v1, v24
	s_waitcnt lgkmcnt(0)
	s_nop 1
	v_add_f32_dpp v1, v1, v1 row_ror:8 row_mask:0xf bank_mask:0xf
	s_waitcnt lgkmcnt(0)
	s_nop 1
	v_add_f32_dpp v1, v1, v1 row_ror:4 row_mask:0xf bank_mask:0xf
	v_mov_b32_e32 v24, v64
	v_mov_b32_e32 v25, v65
	v_mov_b32_e32 v26, v66
	v_mov_b32_e32 v27, v67
	v_mov_b32_e32 v28, v68
	v_mov_b32_e32 v29, v69
	v_mov_b32_e32 v30, v70
	v_mov_b32_e32 v31, v71
	s_waitcnt lgkmcnt(0)
	s_nop 1
	v_add_f32_dpp v1, v1, v1 row_ror:2 row_mask:0xf bank_mask:0xf
	global_store_dwordx4 v[6:7], v[8:11], off
	global_store_dwordx4 v[6:7], v[12:15], off offset:1024
	global_store_dwordx4 v[6:7], v[16:19], off offset:2048
	global_store_dwordx4 v[6:7], v[20:23], off offset:3072
	s_waitcnt lgkmcnt(0)
	s_nop 1
	v_add_f32_dpp v1, v1, v1 row_ror:1 row_mask:0xf bank_mask:0xf
	v_mov_b32_e32 v32, 0x3727c5ac
	v_fmac_f32_e32 v32, 0x3a800000, v1
	v_mul_f32_e32 v1, 0x4f800000, v32
	v_cmp_gt_f32_e32 vcc, s0, v32
	v_mov_b32_e32 v12, v80
	v_mov_b32_e32 v13, v81
	v_mov_b32_e32 v14, v82
	v_mov_b32_e32 v15, v83
	v_mov_b32_e32 v16, v84
	v_mov_b32_e32 v17, v85
	v_mov_b32_e32 v18, v86
	v_mov_b32_e32 v19, v87
	v_cndmask_b32_e32 v1, v32, v1, vcc
	v_sqrt_f32_e32 v32, v1
	v_mov_b32_e32 v8, v72
	v_mov_b32_e32 v9, v73
	v_mov_b32_e32 v10, v74
	v_mov_b32_e32 v11, v75
	v_add_u32_e32 v6, -1, v32
	v_fma_f32 v7, -v6, v32, v1
	v_cmp_ge_f32_e64 s[0:1], 0, v7
	v_add_u32_e32 v7, 1, v32
	v_fma_f32 v20, -v7, v32, v1
	v_cndmask_b32_e64 v6, v32, v6, s[0:1]
	v_cmp_lt_f32_e64 s[0:1], 0, v20
	v_mov_b32_e32 v20, v88
	v_mov_b32_e32 v21, v89
	v_mov_b32_e32 v22, v90
	v_mov_b32_e32 v23, v91
	s_nop 0
	v_cndmask_b32_e64 v6, v6, v7, s[0:1]
	v_mul_f32_e32 v7, 0x37800000, v6
	v_cndmask_b32_e32 v6, v6, v7, vcc
	v_mov_b32_e32 v7, 0x260
	v_cmp_class_f32_e32 vcc, v1, v7
	s_nop 1
	v_cndmask_b32_e32 v1, v6, v1, vcc
	v_div_scale_f32 v32, s[0:1], v1, v1, 1.0
	v_rcp_f32_e32 v33, v32
	v_lshl_add_u64 v[6:7], v[2:3], 0, v[4:5]
	v_div_scale_f32 v34, vcc, 1.0, v1, 1.0
	v_fma_f32 v2, -v32, v33, 1.0
	v_fmac_f32_e32 v33, v2, v33
	v_mul_f32_e32 v35, v34, v33
	v_fma_f32 v2, -v32, v35, v34
	v_fmac_f32_e32 v35, v2, v33
	v_fma_f32 v32, -v32, v35, v34
	v_mov_b32_e32 v2, v76
	v_mov_b32_e32 v3, v77
	v_mov_b32_e32 v4, v78
	v_mov_b32_e32 v5, v79
	v_div_fmas_f32 v52, v32, v33, v35
	v_mov_b32_e32 v32, v92
	v_mov_b32_e32 v33, v93
	v_mov_b32_e32 v34, v94
	v_mov_b32_e32 v35, v95
	v_div_fixup_f32 v0, v52, v1, 1.0
	v_pk_mul_f32 v[36:37], v[36:37], v[0:1] op_sel_hi:[1,0]
	s_waitcnt vmcnt(5)
	v_pk_fma_f32 v[12:13], v[24:25], v[36:37], v[12:13]
	v_pk_mul_f32 v[24:25], v[38:39], v[0:1] op_sel_hi:[1,0]
	v_cvt_pk_f16_f32 v12, v12, v13
	v_pk_fma_f32 v[14:15], v[26:27], v[24:25], v[14:15]
	s_nop 0
	v_cvt_pk_f16_f32 v13, v14, v15
	global_store_dwordx2 v[6:7], v[12:13], off
	v_pk_mul_f32 v[12:13], v[40:41], v[0:1] op_sel_hi:[1,0]
	v_pk_mul_f32 v[14:15], v[42:43], v[0:1] op_sel_hi:[1,0]
	s_waitcnt vmcnt(5)
	v_pk_fma_f32 v[12:13], v[28:29], v[12:13], v[16:17]
	v_pk_fma_f32 v[14:15], v[30:31], v[14:15], v[18:19]
	v_cvt_pk_f16_f32 v12, v12, v13
	v_cvt_pk_f16_f32 v13, v14, v15
	global_store_dwordx2 v[6:7], v[12:13], off offset:512
	v_pk_mul_f32 v[12:13], v[44:45], v[0:1] op_sel_hi:[1,0]
	s_waitcnt vmcnt(4)
	v_pk_fma_f32 v[8:9], v[12:13], v[8:9], v[20:21]
	v_pk_mul_f32 v[12:13], v[46:47], v[0:1] op_sel_hi:[1,0]
	v_cvt_pk_f16_f32 v8, v8, v9
	v_pk_fma_f32 v[10:11], v[12:13], v[10:11], v[22:23]
	s_nop 0
	v_cvt_pk_f16_f32 v9, v10, v11
	global_store_dwordx2 v[6:7], v[8:9], off offset:1024
	v_pk_mul_f32 v[8:9], v[48:49], v[0:1] op_sel_hi:[1,0]
	v_pk_mul_f32 v[0:1], v[50:51], v[0:1] op_sel_hi:[1,0]
	s_waitcnt vmcnt(3)
	v_pk_fma_f32 v[2:3], v[8:9], v[2:3], v[32:33]
	v_pk_fma_f32 v[0:1], v[0:1], v[4:5], v[34:35]
	v_cvt_pk_f16_f32 v2, v2, v3
	v_cvt_pk_f16_f32 v3, v0, v1
	global_store_dwordx2 v[6:7], v[2:3], off offset:1536
	s_endpgm
	s_endpgm
	s_endpgm
	s_endpgm
	s_endpgm
	s_endpgm
	s_endpgm
	s_endpgm
	s_endpgm
	s_endpgm
	s_endpgm
	s_endpgm
	s_endpgm
	s_endpgm
	s_endpgm
	s_endpgm
	s_endpgm
	s_endpgm
	s_endpgm
	s_endpgm
	s_endpgm
	s_endpgm
	s_endpgm
	s_endpgm
	s_endpgm
	s_endpgm
	s_endpgm
	s_endpgm
	s_endpgm
	s_endpgm
	s_endpgm
	s_endpgm
	s_endpgm
	s_endpgm
	s_endpgm
	s_endpgm
	s_endpgm
	s_endpgm
	s_endpgm
	s_endpgm
	s_endpgm
	s_endpgm

	.amdhsa_kernel _Z9ln_kernelILi2EEvPKiPKfS3_PfS3_S3_PDF16_
		.amdhsa_group_segment_fixed_size 0
		.amdhsa_private_segment_fixed_size 0
		.amdhsa_kernarg_size 56
		.amdhsa_user_sgpr_count 2
		.amdhsa_user_sgpr_dispatch_ptr 0
		.amdhsa_user_sgpr_queue_ptr 0
		.amdhsa_user_sgpr_kernarg_segment_ptr 1
		.amdhsa_user_sgpr_dispatch_id 0
		.amdhsa_user_sgpr_kernarg_preload_length 0
		.amdhsa_user_sgpr_kernarg_preload_offset 0
		.amdhsa_user_sgpr_private_segment_size 0
		.amdhsa_uses_dynamic_stack 0
		.amdhsa_enable_private_segment 0
		.amdhsa_system_sgpr_workgroup_id_x 1
		.amdhsa_system_sgpr_workgroup_id_y 0
		.amdhsa_system_sgpr_workgroup_id_z 0
		.amdhsa_system_sgpr_workgroup_info 0
		.amdhsa_system_vgpr_workitem_id 0
		.amdhsa_next_free_vgpr 96
		.amdhsa_next_free_sgpr 16
		.amdhsa_accum_offset 96
		.amdhsa_reserve_vcc 1
		.amdhsa_float_round_mode_32 0
		.amdhsa_float_round_mode_16_64 0
		.amdhsa_float_denorm_mode_32 3
		.amdhsa_float_denorm_mode_16_64 3
		.amdhsa_dx10_clamp 1
		.amdhsa_ieee_mode 1
		.amdhsa_fp16_overflow 0
		.amdhsa_tg_split 0
		.amdhsa_exception_fp_ieee_invalid_op 0
		.amdhsa_exception_fp_denorm_src 0
		.amdhsa_exception_fp_ieee_div_zero 0
		.amdhsa_exception_fp_ieee_overflow 0
		.amdhsa_exception_fp_ieee_underflow 0
		.amdhsa_exception_fp_ieee_inexact 0
		.amdhsa_exception_int_div_zero 0
	.end_amdhsa_kernel

_Z9ln_kernelILi0EEvPKiPKfS3_PfS3_S3_PDF16_:
	s_load_dwordx4 s[12:15], s[0:1], 0x20
	v_and_b32_e32 v62, 63, v0
	v_lshlrev_b32_e32 v62, 4, v62
	s_load_dwordx8 s[4:11], s[0:1], 0x18
	v_and_b32_e32 v52, 63, v0
	v_lshrrev_b32_e32 v0, 6, v0
	v_lshl_or_b32 v0, s2, 2, v0
	v_ashrrev_i32_e32 v1, 31, v0
	v_lshlrev_b64 v[2:3], 12, v[0:1]
	s_waitcnt lgkmcnt(0)
	global_load_dwordx4 v[64:67], v62, s[12:13]
	global_load_dwordx4 v[68:71], v62, s[12:13] offset:1024
	global_load_dwordx4 v[72:75], v62, s[12:13] offset:2048
	global_load_dwordx4 v[76:79], v62, s[12:13] offset:3072
	global_load_dwordx4 v[80:83], v62, s[14:15]
	global_load_dwordx4 v[84:87], v62, s[14:15] offset:1024
	global_load_dwordx4 v[88:91], v62, s[14:15] offset:2048
	global_load_dwordx4 v[92:95], v62, s[14:15] offset:3072
	v_lshl_add_u64 v[4:5], s[4:5], 0, v[2:3]
	v_lshlrev_b32_e32 v2, 4, v52
	v_mov_b32_e32 v3, 0
	v_lshl_add_u64 v[20:21], v[4:5], 0, v[2:3]
	global_load_dwordx4 v[4:7], v[20:21], off offset:1024
	global_load_dwordx4 v[8:11], v[20:21], off offset:2048
	global_load_dwordx4 v[12:15], v[20:21], off
	global_load_dwordx4 v[16:19], v[20:21], off offset:3072
	v_mbcnt_lo_u32_b32 v20, -1, 0
	v_mbcnt_hi_u32_b32 v32, -1, v20
	v_and_b32_e32 v20, 64, v32
	v_xor_b32_e32 v21, 32, v32
	v_add_u32_e32 v34, 64, v20
	v_cmp_lt_i32_e32 vcc, v21, v34
	v_xor_b32_e32 v33, 16, v32
	s_mov_b32 s0, 0xf800000
	v_cndmask_b32_e32 v20, v32, v21, vcc
	v_lshlrev_b32_e32 v53, 2, v20
	v_cmp_lt_i32_e32 vcc, v33, v34
	v_lshlrev_b64 v[0:1], 11, v[0:1]
	v_lshl_add_u64 v[0:1], s[10:11], 0, v[0:1]
	s_waitcnt vmcnt(3)
	v_mov_b32_e32 v36, v5
	v_mov_b32_e32 v37, v6
	v_mov_b32_e32 v5, v7
	s_waitcnt vmcnt(1)
	v_mov_b32_e32 v22, v12
	v_mov_b32_e32 v23, v14
	v_mov_b32_e32 v24, v13
	v_mov_b32_e32 v25, v15
	v_mov_b32_e32 v6, v9
	v_mov_b32_e32 v20, v11
	s_waitcnt vmcnt(0)
	v_mov_b32_e32 v21, v16
	v_pk_add_f32 v[26:27], v[36:37], v[4:5]
	v_pk_add_f32 v[22:23], v[22:23], v[24:25]
	v_pk_add_f32 v[28:29], v[8:9], v[6:7]
	v_pk_add_f32 v[30:31], v[10:11], v[20:21]
	v_pk_add_f32 v[24:25], v[26:27], v[26:27] op_sel:[0,1] op_sel_hi:[1,0]
	v_add_f32_e32 v5, v22, v23
	v_mov_b32_e32 v29, v18
	v_mov_b32_e32 v31, v19
	v_add_f32_e32 v20, 0, v5
	v_mov_b32_e32 v25, v17
	v_pk_add_f32 v[22:23], v[28:29], v[30:31]
	v_pk_add_f32 v[20:21], v[20:21], v[24:25]
	v_pk_mov_b32 v[36:37], v[36:37], v[36:37] op_sel:[1,0]
	v_pk_add_f32 v[20:21], v[20:21], v[22:23]
	s_nop 0
	v_add_f32_e32 v5, v20, v21
	ds_bpermute_b32 v6, v53, v5
	v_cndmask_b32_e32 v21, v32, v33, vcc
	v_lshlrev_b32_e32 v54, 2, v21
	v_xor_b32_e32 v20, 8, v32
	v_cmp_lt_i32_e32 vcc, v20, v34
	s_waitcnt lgkmcnt(0)
	v_add_f32_e32 v5, v5, v6
	ds_bpermute_b32 v6, v54, v5
	v_cndmask_b32_e32 v20, v32, v20, vcc
	v_lshlrev_b32_e32 v55, 2, v20
	v_xor_b32_e32 v21, 4, v32
	v_cmp_lt_i32_e32 vcc, v21, v34
	s_waitcnt lgkmcnt(0)
	v_add_f32_e32 v5, v5, v6
	v_cndmask_b32_e32 v21, v32, v21, vcc
	v_lshlrev_b32_e32 v56, 2, v21
	v_xor_b32_e32 v20, 2, v32
	v_cmp_lt_i32_e32 vcc, v20, v34
	s_waitcnt lgkmcnt(0)
	s_nop 1
	v_add_f32_dpp v5, v5, v5 row_ror:8 row_mask:0xf bank_mask:0xf
	v_cndmask_b32_e32 v20, v32, v20, vcc
	v_lshlrev_b32_e32 v57, 2, v20
	v_xor_b32_e32 v21, 1, v32
	v_cmp_lt_i32_e32 vcc, v21, v34
	s_waitcnt lgkmcnt(0)
	s_nop 1
	v_add_f32_dpp v5, v5, v5 row_ror:4 row_mask:0xf bank_mask:0xf
	v_cndmask_b32_e32 v20, v32, v21, vcc
	v_lshlrev_b32_e32 v58, 2, v20
	v_mov_b32_e32 v20, v64
	v_mov_b32_e32 v21, v65
	v_mov_b32_e32 v22, v66
	v_mov_b32_e32 v23, v67
	v_mov_b32_e32 v24, v80
	v_mov_b32_e32 v25, v81
	v_mov_b32_e32 v26, v82
	v_mov_b32_e32 v27, v83
	v_mov_b32_e32 v28, v68
	v_mov_b32_e32 v29, v69
	v_mov_b32_e32 v30, v70
	v_mov_b32_e32 v31, v71
	v_mov_b32_e32 v32, v84
	v_mov_b32_e32 v33, v85
	v_mov_b32_e32 v34, v86
	v_mov_b32_e32 v35, v87
	s_waitcnt lgkmcnt(0)
	s_nop 1
	v_add_f32_dpp v6, v5, v5 row_ror:2 row_mask:0xf bank_mask:0xf
	v_mov_b32_e32 v5, v37
	v_mov_b32_e32 v37, v7
	s_waitcnt lgkmcnt(0)
	s_nop 1
	v_add_f32_dpp v6, v6, v6 row_ror:1 row_mask:0xf bank_mask:0xf
	v_mul_f32_e32 v6, 0x3a800000, v6
	v_pk_add_f32 v[38:39], v[12:13], v[6:7] op_sel_hi:[1,0] neg_lo:[0,1] neg_hi:[0,1]
	v_pk_add_f32 v[40:41], v[14:15], v[6:7] op_sel_hi:[1,0] neg_lo:[0,1] neg_hi:[0,1]
	v_pk_add_f32 v[46:47], v[4:5], v[6:7] op_sel_hi:[1,0] neg_lo:[0,1] neg_hi:[0,1]
	v_pk_add_f32 v[36:37], v[36:37], v[6:7] op_sel_hi:[1,0] neg_lo:[0,1] neg_hi:[0,1]
	v_pk_add_f32 v[42:43], v[16:17], v[6:7] op_sel_hi:[1,0] neg_lo:[0,1] neg_hi:[0,1]
	v_pk_add_f32 v[44:45], v[18:19], v[6:7] op_sel_hi:[1,0] neg_lo:[0,1] neg_hi:[0,1]
	v_pk_add_f32 v[48:49], v[8:9], v[6:7] op_sel_hi:[1,0] neg_lo:[0,1] neg_hi:[0,1]
	v_pk_add_f32 v[50:51], v[10:11], v[6:7] op_sel_hi:[1,0] neg_lo:[0,1] neg_hi:[0,1]
	v_mov_b32_e32 v6, v39
	v_mov_b32_e32 v7, v41
	v_mov_b32_e32 v14, v47
	v_mov_b32_e32 v15, v37
	v_mov_b32_e32 v4, v38
	v_mov_b32_e32 v5, v40
	v_mov_b32_e32 v12, v46
	v_mov_b32_e32 v13, v36
	v_pk_mul_f32 v[6:7], v[6:7], v[6:7]
	v_pk_mul_f32 v[14:15], v[14:15], v[14:15]
	v_mul_f32_e32 v16, v48, v48
	v_mul_f32_e32 v18, v50, v50
	v_pk_fma_f32 v[4:5], v[4:5], v[4:5], v[6:7]
	v_pk_fma_f32 v[6:7], v[12:13], v[12:13], v[14:15]
	v_pk_mul_f32 v[8:9], v[42:43], v[42:43]
	v_pk_mul_f32 v[10:11], v[44:45], v[44:45]
	v_pk_fma_f32 v[16:17], v[48:49], v[48:49], v[16:17] op_sel_hi:[1,1,0]
	v_pk_fma_f32 v[18:19], v[50:51], v[50:51], v[18:19] op_sel_hi:[1,1,0]
	v_pk_add_f32 v[4:5], v[4:5], v[4:5] op_sel_hi:[0,1]
	v_pk_add_f32 v[6:7], v[6:7], v[6:7] op_sel_hi:[0,1]
	v_mov_b32_e32 v16, v8
	v_mov_b32_e32 v18, v9
	v_mov_b32_e32 v4, v10
	v_mov_b32_e32 v6, v11
	v_pk_add_f32 v[8:9], v[16:17], v[18:19]
	v_pk_add_f32 v[4:5], v[4:5], v[6:7]
	s_nop 0
	v_pk_add_f32 v[4:5], v[8:9], v[4:5]
	s_nop 0
	v_add_f32_e32 v59, v4, v5
	v_mov_b32_e32 v4, v72
	v_mov_b32_e32 v5, v73
	v_mov_b32_e32 v6, v74
	v_mov_b32_e32 v7, v75
	v_mov_b32_e32 v8, v88
	v_mov_b32_e32 v9, v89
	v_mov_b32_e32 v10, v90
	v_mov_b32_e32 v11, v91
	v_mov_b32_e32 v12, v76
	v_mov_b32_e32 v13, v77
	v_mov_b32_e32 v14, v78
	v_mov_b32_e32 v15, v79
	v_mov_b32_e32 v16, v92
	v_mov_b32_e32 v17, v93
	v_mov_b32_e32 v18, v94
	v_mov_b32_e32 v19, v95
	ds_bpermute_b32 v53, v53, v59
	s_waitcnt lgkmcnt(0)
	v_add_f32_e32 v2, v59, v53
	ds_bpermute_b32 v53, v54, v2
	v_mov_b32_e32 v54, 0x3727c5ac
	s_waitcnt lgkmcnt(0)
	v_add_f32_e32 v2, v2, v53
	v_mov_b32_e32 v55, 0x260
	s_waitcnt lgkmcnt(0)
	s_nop 1
	v_add_f32_dpp v2, v2, v2 row_ror:8 row_mask:0xf bank_mask:0xf
	s_waitcnt lgkmcnt(0)
	s_nop 1
	v_add_f32_dpp v2, v2, v2 row_ror:4 row_mask:0xf bank_mask:0xf
	s_waitcnt lgkmcnt(0)
	s_nop 1
	v_add_f32_dpp v2, v2, v2 row_ror:2 row_mask:0xf bank_mask:0xf
	s_waitcnt lgkmcnt(0)
	s_nop 1
	v_add_f32_dpp v2, v2, v2 row_ror:1 row_mask:0xf bank_mask:0xf
	v_fmac_f32_e32 v54, 0x3a800000, v2
	v_mul_f32_e32 v2, 0x4f800000, v54
	v_cmp_gt_f32_e32 vcc, s0, v54
	s_nop 1
	v_cndmask_b32_e32 v53, v54, v2, vcc
	v_sqrt_f32_e32 v54, v53
	v_lshlrev_b32_e32 v2, 3, v52
	v_lshl_add_u64 v[0:1], v[0:1], 0, v[2:3]
	v_add_u32_e32 v52, -1, v54
	v_add_u32_e32 v56, 1, v54
	v_fma_f32 v57, -v52, v54, v53
	v_fma_f32 v58, -v56, v54, v53
	v_cmp_ge_f32_e64 s[0:1], 0, v57
	s_nop 1
	v_cndmask_b32_e64 v52, v54, v52, s[0:1]
	v_cmp_lt_f32_e64 s[0:1], 0, v58
	s_nop 1
	v_cndmask_b32_e64 v52, v52, v56, s[0:1]
	v_mul_f32_e32 v54, 0x37800000, v52
	v_cndmask_b32_e32 v52, v52, v54, vcc
	v_cmp_class_f32_e32 vcc, v53, v55
	s_nop 1
	v_cndmask_b32_e32 v52, v52, v53, vcc
	v_div_scale_f32 v53, s[0:1], v52, v52, 1.0
	v_rcp_f32_e32 v54, v53
	v_div_scale_f32 v2, vcc, 1.0, v52, 1.0
	v_fma_f32 v3, -v53, v54, 1.0
	v_fmac_f32_e32 v54, v3, v54
	v_mul_f32_e32 v3, v2, v54
	v_fma_f32 v55, -v53, v3, v2
	v_fmac_f32_e32 v3, v55, v54
	v_fma_f32 v2, -v53, v3, v2
	v_div_fmas_f32 v2, v2, v54, v3
	v_div_fixup_f32 v2, v2, v52, 1.0
	v_pk_mul_f32 v[38:39], v[38:39], v[2:3] op_sel_hi:[1,0]
	v_pk_mul_f32 v[40:41], v[40:41], v[2:3] op_sel_hi:[1,0]
	v_pk_mul_f32 v[46:47], v[46:47], v[2:3] op_sel_hi:[1,0]
	v_pk_mul_f32 v[36:37], v[36:37], v[2:3] op_sel_hi:[1,0]
	v_pk_mul_f32 v[48:49], v[48:49], v[2:3] op_sel_hi:[1,0]
	v_pk_mul_f32 v[50:51], v[50:51], v[2:3] op_sel_hi:[1,0]
	v_pk_mul_f32 v[42:43], v[42:43], v[2:3] op_sel_hi:[1,0]
	v_pk_mul_f32 v[2:3], v[44:45], v[2:3] op_sel_hi:[1,0]
	s_waitcnt vmcnt(6)
	v_pk_fma_f32 v[20:21], v[20:21], v[38:39], v[24:25]
	v_pk_fma_f32 v[22:23], v[22:23], v[40:41], v[26:27]
	s_waitcnt vmcnt(4)
	v_pk_fma_f32 v[24:25], v[28:29], v[46:47], v[32:33]
	v_pk_fma_f32 v[26:27], v[30:31], v[36:37], v[34:35]
	s_waitcnt vmcnt(2)
	v_pk_fma_f32 v[4:5], v[48:49], v[4:5], v[8:9]
	v_pk_fma_f32 v[6:7], v[50:51], v[6:7], v[10:11]
	s_waitcnt vmcnt(0)
	v_pk_fma_f32 v[8:9], v[42:43], v[12:13], v[16:17]
	v_pk_fma_f32 v[2:3], v[2:3], v[14:15], v[18:19]
	v_cvt_pk_f16_f32 v10, v20, v21
	v_cvt_pk_f16_f32 v11, v22, v23
	v_cvt_pk_f16_f32 v12, v24, v25
	v_cvt_pk_f16_f32 v13, v26, v27
	v_cvt_pk_f16_f32 v4, v4, v5
	v_cvt_pk_f16_f32 v5, v6, v7
	v_cvt_pk_f16_f32 v6, v8, v9
	v_cvt_pk_f16_f32 v7, v2, v3
	global_store_dwordx2 v[0:1], v[10:11], off
	global_store_dwordx2 v[0:1], v[12:13], off offset:512
	global_store_dwordx2 v[0:1], v[4:5], off offset:1024
	global_store_dwordx2 v[0:1], v[6:7], off offset:1536
	s_endpgm
	s_endpgm
	s_endpgm
	s_endpgm
	s_endpgm
	s_endpgm
	s_endpgm
	s_endpgm

	.amdhsa_kernel _Z9ln_kernelILi0EEvPKiPKfS3_PfS3_S3_PDF16_
		.amdhsa_group_segment_fixed_size 0
		.amdhsa_private_segment_fixed_size 0
		.amdhsa_kernarg_size 56
		.amdhsa_user_sgpr_count 2
		.amdhsa_user_sgpr_dispatch_ptr 0
		.amdhsa_user_sgpr_queue_ptr 0
		.amdhsa_user_sgpr_kernarg_segment_ptr 1
		.amdhsa_user_sgpr_dispatch_id 0
		.amdhsa_user_sgpr_kernarg_preload_length 0
		.amdhsa_user_sgpr_kernarg_preload_offset 0
		.amdhsa_user_sgpr_private_segment_size 0
		.amdhsa_uses_dynamic_stack 0
		.amdhsa_enable_private_segment 0
		.amdhsa_system_sgpr_workgroup_id_x 1
		.amdhsa_system_sgpr_workgroup_id_y 0
		.amdhsa_system_sgpr_workgroup_id_z 0
		.amdhsa_system_sgpr_workgroup_info 0
		.amdhsa_system_vgpr_workitem_id 0
		.amdhsa_next_free_vgpr 96
		.amdhsa_next_free_sgpr 16
		.amdhsa_accum_offset 96
		.amdhsa_reserve_vcc 1
		.amdhsa_float_round_mode_32 0
		.amdhsa_float_round_mode_16_64 0
		.amdhsa_float_denorm_mode_32 3
		.amdhsa_float_denorm_mode_16_64 3
		.amdhsa_dx10_clamp 1
		.amdhsa_ieee_mode 1
		.amdhsa_fp16_overflow 0
		.amdhsa_tg_split 0
		.amdhsa_exception_fp_ieee_invalid_op 0
		.amdhsa_exception_fp_denorm_src 0
		.amdhsa_exception_fp_ieee_div_zero 0
		.amdhsa_exception_fp_ieee_overflow 0
		.amdhsa_exception_fp_ieee_underflow 0
		.amdhsa_exception_fp_ieee_inexact 0
		.amdhsa_exception_int_div_zero 0
	.end_amdhsa_kernel

amdhsa.kernels:
  - .agpr_count:     0
    .args:
      - .offset:         0
        .size:           400
        .value_kind:     by_value
    .group_segment_fixed_size: 33280
    .kernarg_segment_align: 8
    .kernarg_segment_size: 400
    .language:       OpenCL C
    .language_version:
      - 2
      - 0
    .max_flat_workgroup_size: 256
    .name:           _Z10wt_convert7CvtJobs
    .private_segment_fixed_size: 0
    .sgpr_count:     54
    .sgpr_spill_count: 0
    .symbol:         _Z10wt_convert7CvtJobs.kd
    .uniform_work_group_size: 1
    .uses_dynamic_stack: false
    .vgpr_count:     45
    .vgpr_spill_count: 0
    .wavefront_size: 64
  - .agpr_count:     0
    .args:
      - .actual_access:  read_only
        .address_space:  global
        .offset:         0
        .size:           8
        .value_kind:     global_buffer
      - .actual_access:  read_only
        .address_space:  global
        .offset:         8
        .size:           8
        .value_kind:     global_buffer
      - .actual_access:  read_only
        .address_space:  global
        .offset:         16
        .size:           8
        .value_kind:     global_buffer
      - .actual_access:  write_only
        .address_space:  global
        .offset:         24
        .size:           8
        .value_kind:     global_buffer
      - .actual_access:  read_only
        .address_space:  global
        .offset:         32
        .size:           8
        .value_kind:     global_buffer
      - .actual_access:  read_only
        .address_space:  global
        .offset:         40
        .size:           8
        .value_kind:     global_buffer
      - .actual_access:  write_only
        .address_space:  global
        .offset:         48
        .size:           8
        .value_kind:     global_buffer
      - .offset:         56
        .size:           400
        .value_kind:     by_value
    .group_segment_fixed_size: 33280
    .kernarg_segment_align: 8
    .kernarg_segment_size: 456
    .language:       OpenCL C
    .language_version:
      - 2
      - 0
    .max_flat_workgroup_size: 256
    .name:           _Z13embed_ln_convPKiPKfS2_PfS2_S2_PDF16_7CvtJobs
    .private_segment_fixed_size: 0
    .sgpr_count:     36
    .sgpr_spill_count: 0
    .symbol:         _Z13embed_ln_convPKiPKfS2_PfS2_S2_PDF16_7CvtJobs.kd
    .uniform_work_group_size: 1
    .uses_dynamic_stack: false
    .vgpr_count:     79
    .vgpr_spill_count: 0
    .wavefront_size: 64
  - .agpr_count:     0
    .args:
      - .address_space:  global
        .offset:         0
        .size:           8
        .value_kind:     global_buffer
      - .address_space:  global
        .offset:         8
        .size:           8
        .value_kind:     global_buffer
      - .actual_access:  write_only
        .address_space:  global
        .offset:         16
        .size:           8
        .value_kind:     global_buffer
      - .actual_access:  read_only
        .address_space:  global
        .offset:         24
        .size:           8
        .value_kind:     global_buffer
      - .offset:         32
        .size:           4
        .value_kind:     by_value
      - .offset:         36
        .size:           4
        .value_kind:     by_value
      - .offset:         40
        .size:           4
        .value_kind:     by_value
    .group_segment_fixed_size: 0
    .kernarg_segment_align: 8
    .kernarg_segment_size: 44
    .language:       OpenCL C
    .language_version:
      - 2
      - 0
    .max_flat_workgroup_size: 512
    .name:           _Z17gemm_256sq_8phasePKDF16_S0_PfPKfiii
    .private_segment_fixed_size: 0
    .sgpr_count:     47
    .sgpr_spill_count: 0
    .symbol:         _Z17gemm_256sq_8phasePKDF16_S0_PfPKfiii.kd
    .uniform_work_group_size: 1
    .uses_dynamic_stack: false
    .vgpr_count:     244
    .vgpr_spill_count: 0
    .wavefront_size: 64
  - .agpr_count:     0
    .args:
      - .actual_access:  read_only
        .address_space:  global
        .offset:         0
        .size:           8
        .value_kind:     global_buffer
      - .actual_access:  read_only
        .address_space:  global
        .offset:         8
        .size:           8
        .value_kind:     global_buffer
      - .actual_access:  read_only
        .address_space:  global
        .offset:         16
        .size:           8
        .value_kind:     global_buffer
      - .actual_access:  write_only
        .address_space:  global
        .offset:         24
        .size:           8
        .value_kind:     global_buffer
      - .offset:         32
        .size:           400
        .value_kind:     by_value
    .group_segment_fixed_size: 33280
    .kernarg_segment_align: 8
    .kernarg_segment_size: 432
    .language:       OpenCL C
    .language_version:
      - 2
      - 0
    .max_flat_workgroup_size: 256
    .name:           _Z11attn_kernelPKDF16_S0_S0_PDF16_7CvtJobs
    .private_segment_fixed_size: 0
    .sgpr_count:     36
    .sgpr_spill_count: 0
    .symbol:         _Z11attn_kernelPKDF16_S0_S0_PDF16_7CvtJobs.kd
    .uniform_work_group_size: 1
    .uses_dynamic_stack: false
    .vgpr_count:     116
    .vgpr_spill_count: 0
    .wavefront_size: 64
  - .agpr_count:     0
    .args:
      - .address_space:  global
        .offset:         0
        .size:           8
        .value_kind:     global_buffer
      - .address_space:  global
        .offset:         8
        .size:           8
        .value_kind:     global_buffer
      - .offset:         16
        .size:           4
        .value_kind:     by_value
      - .offset:         20
        .size:           4
        .value_kind:     by_value
      - .offset:         24
        .size:           4
        .value_kind:     by_value
      - .actual_access:  write_only
        .address_space:  global
        .offset:         32
        .size:           8
        .value_kind:     global_buffer
      - .actual_access:  read_only
        .address_space:  global
        .offset:         40
        .size:           8
        .value_kind:     global_buffer
      - .actual_access:  read_only
        .address_space:  global
        .offset:         48
        .size:           8
        .value_kind:     global_buffer
      - .offset:         56
        .size:           4
        .value_kind:     hidden_block_count_x
      - .offset:         60
        .size:           4
        .value_kind:     hidden_block_count_y
      - .offset:         64
        .size:           4
        .value_kind:     hidden_block_count_z
      - .offset:         68
        .size:           2
        .value_kind:     hidden_group_size_x
      - .offset:         70
        .size:           2
        .value_kind:     hidden_group_size_y
      - .offset:         72
        .size:           2
        .value_kind:     hidden_group_size_z
      - .offset:         74
        .size:           2
        .value_kind:     hidden_remainder_x
      - .offset:         76
        .size:           2
        .value_kind:     hidden_remainder_y
      - .offset:         78
        .size:           2
        .value_kind:     hidden_remainder_z
      - .offset:         96
        .size:           8
        .value_kind:     hidden_global_offset_x
      - .offset:         104
        .size:           8
        .value_kind:     hidden_global_offset_y
      - .offset:         112
        .size:           8
        .value_kind:     hidden_global_offset_z
      - .offset:         120
        .size:           2
        .value_kind:     hidden_grid_dims
      - .offset:         176
        .size:           4
        .value_kind:     hidden_dynamic_lds_size
    .group_segment_fixed_size: 0
    .kernarg_segment_align: 8
    .kernarg_segment_size: 312
    .language:       OpenCL C
    .language_version:
      - 2
      - 0
    .max_flat_workgroup_size: 512
    .name:           _Z5gemm8ILi192ELi2ELi3ELi0ELi1ELi16EEvPKDF16_S1_iiiPDF16_PfPKf
    .private_segment_fixed_size: 0
    .sgpr_count:     34
    .sgpr_spill_count: 0
    .symbol:         _Z5gemm8ILi192ELi2ELi3ELi0ELi1ELi16EEvPKDF16_S1_iiiPDF16_PfPKf.kd
    .uniform_work_group_size: 1
    .uses_dynamic_stack: false
    .vgpr_count:     125
    .vgpr_spill_count: 0
    .wavefront_size: 64
  - .agpr_count:     0
    .args:
      - .address_space:  global
        .offset:         0
        .size:           8
        .value_kind:     global_buffer
      - .address_space:  global
        .offset:         8
        .size:           8
        .value_kind:     global_buffer
      - .offset:         16
        .size:           4
        .value_kind:     by_value
      - .offset:         20
        .size:           4
        .value_kind:     by_value
      - .offset:         24
        .size:           4
        .value_kind:     by_value
      - .actual_access:  write_only
        .address_space:  global
        .offset:         32
        .size:           8
        .value_kind:     global_buffer
      - .actual_access:  read_only
        .address_space:  global
        .offset:         40
        .size:           8
        .value_kind:     global_buffer
      - .actual_access:  read_only
        .address_space:  global
        .offset:         48
        .size:           8
        .value_kind:     global_buffer
      - .offset:         56
        .size:           4
        .value_kind:     hidden_block_count_x
      - .offset:         60
        .size:           4
        .value_kind:     hidden_block_count_y
      - .offset:         64
        .size:           4
        .value_kind:     hidden_block_count_z
      - .offset:         68
        .size:           2
        .value_kind:     hidden_group_size_x
      - .offset:         70
        .size:           2
        .value_kind:     hidden_group_size_y
      - .offset:         72
        .size:           2
        .value_kind:     hidden_group_size_z
      - .offset:         74
        .size:           2
        .value_kind:     hidden_remainder_x
      - .offset:         76
        .size:           2
        .value_kind:     hidden_remainder_y
      - .offset:         78
        .size:           2
        .value_kind:     hidden_remainder_z
      - .offset:         96
        .size:           8
        .value_kind:     hidden_global_offset_x
      - .offset:         104
        .size:           8
        .value_kind:     hidden_global_offset_y
      - .offset:         112
        .size:           8
        .value_kind:     hidden_global_offset_z
      - .offset:         120
        .size:           2
        .value_kind:     hidden_grid_dims
      - .offset:         176
        .size:           4
        .value_kind:     hidden_dynamic_lds_size
    .group_segment_fixed_size: 0
    .kernarg_segment_align: 8
    .kernarg_segment_size: 312
    .language:       OpenCL C
    .language_version:
      - 2
      - 0
    .max_flat_workgroup_size: 512
    .name:           _Z5gemm8ILi128ELi2ELi2ELi2ELi1ELi16EEvPKDF16_S1_iiiPDF16_PfPKf
    .private_segment_fixed_size: 0
    .sgpr_count:     30
    .sgpr_spill_count: 0
    .symbol:         _Z5gemm8ILi128ELi2ELi2ELi2ELi1ELi16EEvPKDF16_S1_iiiPDF16_PfPKf.kd
    .uniform_work_group_size: 1
    .uses_dynamic_stack: false
    .vgpr_count:     90
    .vgpr_spill_count: 0
    .wavefront_size: 64
  - .agpr_count:     0
    .args:
      - .address_space:  global
        .offset:         0
        .size:           8
        .value_kind:     global_buffer
      - .address_space:  global
        .offset:         8
        .size:           8
        .value_kind:     global_buffer
      - .offset:         16
        .size:           4
        .value_kind:     by_value
      - .offset:         20
        .size:           4
        .value_kind:     by_value
      - .offset:         24
        .size:           4
        .value_kind:     by_value
      - .actual_access:  read_only
        .address_space:  global
        .offset:         32
        .size:           8
        .value_kind:     global_buffer
      - .address_space:  global
        .offset:         40
        .size:           8
        .value_kind:     global_buffer
      - .actual_access:  read_only
        .address_space:  global
        .offset:         48
        .size:           8
        .value_kind:     global_buffer
      - .offset:         56
        .size:           4
        .value_kind:     hidden_block_count_x
      - .offset:         60
        .size:           4
        .value_kind:     hidden_block_count_y
      - .offset:         64
        .size:           4
        .value_kind:     hidden_block_count_z
      - .offset:         68
        .size:           2
        .value_kind:     hidden_group_size_x
      - .offset:         70
        .size:           2
        .value_kind:     hidden_group_size_y
      - .offset:         72
        .size:           2
        .value_kind:     hidden_group_size_z
      - .offset:         74
        .size:           2
        .value_kind:     hidden_remainder_x
      - .offset:         76
        .size:           2
        .value_kind:     hidden_remainder_y
      - .offset:         78
        .size:           2
        .value_kind:     hidden_remainder_z
      - .offset:         96
        .size:           8
        .value_kind:     hidden_global_offset_x
      - .offset:         104
        .size:           8
        .value_kind:     hidden_global_offset_y
      - .offset:         112
        .size:           8
        .value_kind:     hidden_global_offset_z
      - .offset:         120
        .size:           2
        .value_kind:     hidden_grid_dims
      - .offset:         176
        .size:           4
        .value_kind:     hidden_dynamic_lds_size
    .group_segment_fixed_size: 0
    .kernarg_segment_align: 8
    .kernarg_segment_size: 312
    .language:       OpenCL C
    .language_version:
      - 2
      - 0
    .max_flat_workgroup_size: 512
    .name:           _Z5gemm8ILi64ELi4ELi6ELi1ELi1ELi16EEvPKDF16_S1_iiiPDF16_PfPKf
    .private_segment_fixed_size: 0
    .sgpr_count:     34
    .sgpr_spill_count: 0
    .symbol:         _Z5gemm8ILi64ELi4ELi6ELi1ELi1ELi16EEvPKDF16_S1_iiiPDF16_PfPKf.kd
    .uniform_work_group_size: 1
    .uses_dynamic_stack: false
    .vgpr_count:     104
    .vgpr_spill_count: 0
    .wavefront_size: 64
  - .agpr_count:     0
    .args:
      - .address_space:  global
        .offset:         0
        .size:           8
        .value_kind:     global_buffer
      - .address_space:  global
        .offset:         8
        .size:           8
        .value_kind:     global_buffer
      - .offset:         16
        .size:           4
        .value_kind:     by_value
      - .offset:         20
        .size:           4
        .value_kind:     by_value
      - .offset:         24
        .size:           4
        .value_kind:     by_value
      - .actual_access:  write_only
        .address_space:  global
        .offset:         32
        .size:           8
        .value_kind:     global_buffer
      - .actual_access:  read_only
        .address_space:  global
        .offset:         40
        .size:           8
        .value_kind:     global_buffer
      - .actual_access:  read_only
        .address_space:  global
        .offset:         48
        .size:           8
        .value_kind:     global_buffer
    .group_segment_fixed_size: 0
    .kernarg_segment_align: 8
    .kernarg_segment_size: 56
    .language:       OpenCL C
    .language_version:
      - 2
      - 0
    .max_flat_workgroup_size: 512
    .name:           _Z5gemm8ILi128ELi2ELi4ELi4ELi2ELi32EEvPKDF16_S1_iiiPDF16_PfPKf
    .private_segment_fixed_size: 0
    .sgpr_count:     38
    .sgpr_spill_count: 0
    .symbol:         _Z5gemm8ILi128ELi2ELi4ELi4ELi2ELi32EEvPKDF16_S1_iiiPDF16_PfPKf.kd
    .uniform_work_group_size: 1
    .uses_dynamic_stack: false
    .vgpr_count:     107
    .vgpr_spill_count: 0
    .wavefront_size: 64
  - .agpr_count:     0
    .args:
      - .actual_access:  read_only
        .address_space:  global
        .offset:         0
        .size:           8
        .value_kind:     global_buffer
      - .actual_access:  read_only
        .address_space:  global
        .offset:         8
        .size:           8
        .value_kind:     global_buffer
      - .actual_access:  read_only
        .address_space:  global
        .offset:         16
        .size:           8
        .value_kind:     global_buffer
      - .address_space:  global
        .offset:         24
        .size:           8
        .value_kind:     global_buffer
      - .actual_access:  read_only
        .address_space:  global
        .offset:         32
        .size:           8
        .value_kind:     global_buffer
      - .actual_access:  read_only
        .address_space:  global
        .offset:         40
        .size:           8
        .value_kind:     global_buffer
      - .actual_access:  write_only
        .address_space:  global
        .offset:         48
        .size:           8
        .value_kind:     global_buffer
    .group_segment_fixed_size: 0
    .kernarg_segment_align: 8
    .kernarg_segment_size: 56
    .language:       OpenCL C
    .language_version:
      - 2
      - 0
    .max_flat_workgroup_size: 256
    .name:           _Z9ln_kernelILi2EEvPKiPKfS3_PfS3_S3_PDF16_
    .private_segment_fixed_size: 0
    .sgpr_count:     22
    .sgpr_spill_count: 0
    .symbol:         _Z9ln_kernelILi2EEvPKiPKfS3_PfS3_S3_PDF16_.kd
    .uniform_work_group_size: 1
    .uses_dynamic_stack: false
    .vgpr_count:     96
    .vgpr_spill_count: 0
    .wavefront_size: 64
  - .agpr_count:     0
    .args:
      - .actual_access:  read_only
        .address_space:  global
        .offset:         0
        .size:           8
        .value_kind:     global_buffer
      - .actual_access:  read_only
        .address_space:  global
        .offset:         8
        .size:           8
        .value_kind:     global_buffer
      - .actual_access:  read_only
        .address_space:  global
        .offset:         16
        .size:           8
        .value_kind:     global_buffer
      - .actual_access:  read_only
        .address_space:  global
        .offset:         24
        .size:           8
        .value_kind:     global_buffer
      - .actual_access:  read_only
        .address_space:  global
        .offset:         32
        .size:           8
        .value_kind:     global_buffer
      - .actual_access:  read_only
        .address_space:  global
        .offset:         40
        .size:           8
        .value_kind:     global_buffer
      - .actual_access:  write_only
        .address_space:  global
        .offset:         48
        .size:           8
        .value_kind:     global_buffer
    .group_segment_fixed_size: 0
    .kernarg_segment_align: 8
    .kernarg_segment_size: 56
    .language:       OpenCL C
    .language_version:
      - 2
      - 0
    .max_flat_workgroup_size: 256
    .name:           _Z9ln_kernelILi0EEvPKiPKfS3_PfS3_S3_PDF16_
    .private_segment_fixed_size: 0
    .sgpr_count:     22
    .sgpr_spill_count: 0
    .symbol:         _Z9ln_kernelILi0EEvPKiPKfS3_PfS3_S3_PDF16_.kd
    .uniform_work_group_size: 1
    .uses_dynamic_stack: false
    .vgpr_count:     96
    .vgpr_spill_count: 0
    .wavefront_size: 64
  - .agpr_count:     0
    .args:
      - .actual_access:  read_only
        .address_space:  global
        .offset:         0
        .size:           8
        .value_kind:     global_buffer
      - .actual_access:  read_only
        .address_space:  global
        .offset:         8
        .size:           8
        .value_kind:     global_buffer
      - .actual_access:  read_only
        .address_space:  global
        .offset:         16
        .size:           8
        .value_kind:     global_buffer
      - .actual_access:  read_only
        .address_space:  global
        .offset:         24
        .size:           8
        .value_kind:     global_buffer
      - .actual_access:  read_only
        .address_space:  global
        .offset:         32
        .size:           8
        .value_kind:     global_buffer
      - .actual_access:  read_only
        .address_space:  global
        .offset:         40
        .size:           8
        .value_kind:     global_buffer
      - .actual_access:  write_only
        .address_space:  global
        .offset:         48
        .size:           8
        .value_kind:     global_buffer
    .group_segment_fixed_size: 0
    .kernarg_segment_align: 8
    .kernarg_segment_size: 56
    .language:       OpenCL C
    .language_version:
      - 2
      - 0
    .max_flat_workgroup_size: 256
    .name:           _Z9ln_kernelILi4EEvPKiPKfS3_PfS3_S3_PDF16_
    .private_segment_fixed_size: 0
    .sgpr_count:     18
    .sgpr_spill_count: 0
    .symbol:         _Z9ln_kernelILi4EEvPKiPKfS3_PfS3_S3_PDF16_.kd
    .uniform_work_group_size: 1
    .uses_dynamic_stack: false
    .vgpr_count:     64
    .vgpr_spill_count: 0
    .wavefront_size: 64
